# GEMM K-loops: s_setprio moved across the barriers and redundant post-barrier lgkmcnt wait removed (shorter MFMA-wave critical path); bf16 MFMA f32 acc as baseline
# speedup vs baseline: 1.0044x; 1.0044x over previous
.LBB0_265:
	s_add_u32 s24, s6, 0xfff00080
	s_addc_u32 s25, s7, -1
	s_add_i32 s28, 0, 0x10000
	s_cmp_eq_u32 s58, 60
	s_cselect_b32 s27, s73, s25
	s_cselect_b32 s26, vcc_lo, s24
	s_cselect_b32 s25, s75, s13
	s_cselect_b32 s24, vcc_hi, s21
	s_add_i32 s71, 0, 0x14000
	v_add_u32_e32 v144, s28, v163
	v_add_u32_e32 v182, s71, v163
	s_waitcnt lgkmcnt(0)
	ds_read_b128 v[132:135], v144
	ds_read_b128 v[136:139], v144 offset:1024
	ds_read_b128 v[140:143], v144 offset:2048
	ds_read_b128 v[144:147], v144 offset:3072
	ds_read_b128 v[148:151], v182
	ds_read_b128 v[152:155], v182 offset:1024
	ds_read_b128 v[178:181], v182 offset:2048
	ds_read_b128 v[186:189], v182 offset:3072
	v_lshl_add_u64 v[182:183], s[6:7], 0, v[174:175]
	s_add_i32 m0, s46, 0xc000
	ds_read_b128 v[190:193], v184
	ds_read_b128 v[194:197], v184 offset:1024
	ds_read_b128 v[198:201], v184 offset:2048
	ds_read_b128 v[202:205], v184 offset:3072
	ds_read_b128 v[222:225], v184 offset:4096
	ds_read_b128 v[226:229], v184 offset:5120
	ds_read_b128 v[230:233], v184 offset:6144
	ds_read_b128 v[234:237], v184 offset:7168
	global_load_lds_dwordx4 v[182:183], off
	v_lshl_add_u64 v[182:183], s[6:7], 0, v[176:177]
	s_add_i32 m0, s46, 0xe000
	s_nop 0
	global_load_lds_dwordx4 v[182:183], off
	s_waitcnt vmcnt(8)
	s_waitcnt lgkmcnt(0)
	s_setprio 1
	s_barrier
	v_mfma_f32_16x16x32_bf16 v[120:123], v[132:135], v[190:193], v[120:123]
	v_mfma_f32_16x16x32_bf16 v[116:119], v[140:143], v[190:193], v[116:119]
	v_mfma_f32_16x16x32_bf16 v[104:107], v[132:135], v[198:201], v[104:107]
	v_mfma_f32_16x16x32_bf16 v[100:103], v[140:143], v[198:201], v[100:103]
	v_mfma_f32_16x16x32_bf16 v[88:91], v[132:135], v[222:225], v[88:91]
	v_mfma_f32_16x16x32_bf16 v[84:87], v[140:143], v[222:225], v[84:87]
	v_mfma_f32_16x16x32_bf16 v[72:75], v[132:135], v[230:233], v[72:75]
	v_mfma_f32_16x16x32_bf16 v[68:71], v[140:143], v[230:233], v[68:71]
	v_mfma_f32_16x16x32_bf16 v[120:123], v[136:139], v[194:197], v[120:123]
	v_mfma_f32_16x16x32_bf16 v[116:119], v[144:147], v[194:197], v[116:119]
	v_mfma_f32_16x16x32_bf16 v[104:107], v[136:139], v[202:205], v[104:107]
	v_mfma_f32_16x16x32_bf16 v[100:103], v[144:147], v[202:205], v[100:103]
	v_mfma_f32_16x16x32_bf16 v[88:91], v[136:139], v[226:229], v[88:91]
	v_mfma_f32_16x16x32_bf16 v[84:87], v[144:147], v[226:229], v[84:87]
	v_mfma_f32_16x16x32_bf16 v[72:75], v[136:139], v[234:237], v[72:75]
	v_mfma_f32_16x16x32_bf16 v[68:71], v[144:147], v[234:237], v[68:71]
	v_mfma_f32_16x16x32_bf16 v[128:131], v[148:151], v[190:193], v[128:131]
	v_mfma_f32_16x16x32_bf16 v[124:127], v[178:181], v[190:193], v[124:127]
	v_mfma_f32_16x16x32_bf16 v[112:115], v[148:151], v[198:201], v[112:115]
	v_mfma_f32_16x16x32_bf16 v[108:111], v[178:181], v[198:201], v[108:111]
	v_mfma_f32_16x16x32_bf16 v[96:99], v[148:151], v[222:225], v[96:99]
	v_mfma_f32_16x16x32_bf16 v[92:95], v[178:181], v[222:225], v[92:95]
	v_mfma_f32_16x16x32_bf16 v[80:83], v[148:151], v[230:233], v[80:83]
	v_mfma_f32_16x16x32_bf16 v[76:79], v[178:181], v[230:233], v[76:79]
	v_mfma_f32_16x16x32_bf16 v[128:131], v[152:155], v[194:197], v[128:131]
	v_mfma_f32_16x16x32_bf16 v[124:127], v[186:189], v[194:197], v[124:127]
	v_mfma_f32_16x16x32_bf16 v[112:115], v[152:155], v[202:205], v[112:115]
	v_mfma_f32_16x16x32_bf16 v[108:111], v[186:189], v[202:205], v[108:111]
	v_mfma_f32_16x16x32_bf16 v[96:99], v[152:155], v[226:229], v[96:99]
	v_mfma_f32_16x16x32_bf16 v[92:95], v[186:189], v[226:229], v[92:95]
	v_mfma_f32_16x16x32_bf16 v[80:83], v[152:155], v[234:237], v[80:83]
	v_mfma_f32_16x16x32_bf16 v[76:79], v[186:189], v[234:237], v[76:79]
	s_barrier
	s_setprio 0
	s_add_i32 s28, s28, s1
	v_lshl_add_u64 v[182:183], s[24:25], 0, v[2:3]
	s_mov_b32 m0, s28
	ds_read_b128 v[190:193], v184 offset:16384
	ds_read_b128 v[194:197], v184 offset:17408
	ds_read_b128 v[198:201], v184 offset:18432
	ds_read_b128 v[202:205], v184 offset:19456
	ds_read_b128 v[222:225], v184 offset:20480
	ds_read_b128 v[226:229], v184 offset:21504
	ds_read_b128 v[230:233], v184 offset:22528
	ds_read_b128 v[234:237], v184 offset:23552
	global_load_lds_dwordx4 v[182:183], off
	s_add_i32 m0, s28, 0x2000
	s_add_u32 s28, s24, 0x100000
	v_lshl_add_u64 v[238:239], s[24:25], 0, v[168:169]
	s_addc_u32 s29, s25, 0
	s_add_i32 s71, s71, s1
	global_load_lds_dwordx4 v[238:239], off
	v_lshl_add_u64 v[240:241], s[28:29], 0, v[2:3]
	s_mov_b32 m0, s71
	v_lshl_add_u64 v[242:243], s[26:27], 0, v[170:171]
	global_load_lds_dwordx4 v[240:241], off
	v_lshl_add_u64 v[240:241], s[28:29], 0, v[168:169]
	s_add_i32 m0, s71, 0x2000
	s_nop 0
	global_load_lds_dwordx4 v[240:241], off
	v_lshl_add_u64 v[240:241], s[26:27], 0, v[172:173]
	s_mov_b32 m0, s46
	s_nop 0
	global_load_lds_dwordx4 v[240:241], off
	s_mov_b32 m0, s50
	s_nop 0
	global_load_lds_dwordx4 v[242:243], off
	s_waitcnt vmcnt(8)
	s_waitcnt lgkmcnt(0)
	s_setprio 1
	s_barrier
	v_mfma_f32_16x16x32_bf16 v[56:59], v[132:135], v[190:193], v[56:59]
	v_mfma_f32_16x16x32_bf16 v[52:55], v[140:143], v[190:193], v[52:55]
	v_mfma_f32_16x16x32_bf16 v[40:43], v[132:135], v[198:201], v[40:43]
	v_mfma_f32_16x16x32_bf16 v[36:39], v[140:143], v[198:201], v[36:39]
	v_mfma_f32_16x16x32_bf16 v[24:27], v[132:135], v[222:225], v[24:27]
	v_mfma_f32_16x16x32_bf16 v[20:23], v[140:143], v[222:225], v[20:23]
	v_mfma_f32_16x16x32_bf16 v[8:11], v[132:135], v[230:233], v[8:11]
	v_mfma_f32_16x16x32_bf16 v[4:7], v[140:143], v[230:233], v[4:7]
	v_mfma_f32_16x16x32_bf16 v[56:59], v[136:139], v[194:197], v[56:59]
	v_mfma_f32_16x16x32_bf16 v[52:55], v[144:147], v[194:197], v[52:55]
	v_mfma_f32_16x16x32_bf16 v[40:43], v[136:139], v[202:205], v[40:43]
	v_mfma_f32_16x16x32_bf16 v[36:39], v[144:147], v[202:205], v[36:39]
	v_mfma_f32_16x16x32_bf16 v[24:27], v[136:139], v[226:229], v[24:27]
	v_mfma_f32_16x16x32_bf16 v[20:23], v[144:147], v[226:229], v[20:23]
	v_mfma_f32_16x16x32_bf16 v[8:11], v[136:139], v[234:237], v[8:11]
	v_mfma_f32_16x16x32_bf16 v[4:7], v[144:147], v[234:237], v[4:7]
	v_mfma_f32_16x16x32_bf16 v[64:67], v[148:151], v[190:193], v[64:67]
	v_mfma_f32_16x16x32_bf16 v[60:63], v[178:181], v[190:193], v[60:63]
	v_mfma_f32_16x16x32_bf16 v[48:51], v[148:151], v[198:201], v[48:51]
	v_mfma_f32_16x16x32_bf16 v[44:47], v[178:181], v[198:201], v[44:47]
	v_mfma_f32_16x16x32_bf16 v[32:35], v[148:151], v[222:225], v[32:35]
	v_mfma_f32_16x16x32_bf16 v[28:31], v[178:181], v[222:225], v[28:31]
	v_mfma_f32_16x16x32_bf16 v[16:19], v[148:151], v[230:233], v[16:19]
	v_mfma_f32_16x16x32_bf16 v[12:15], v[178:181], v[230:233], v[12:15]
	v_mfma_f32_16x16x32_bf16 v[64:67], v[152:155], v[194:197], v[64:67]
	v_mfma_f32_16x16x32_bf16 v[60:63], v[186:189], v[194:197], v[60:63]
	v_mfma_f32_16x16x32_bf16 v[48:51], v[152:155], v[202:205], v[48:51]
	v_mfma_f32_16x16x32_bf16 v[44:47], v[186:189], v[202:205], v[44:47]
	v_mfma_f32_16x16x32_bf16 v[32:35], v[152:155], v[226:229], v[32:35]
	v_mfma_f32_16x16x32_bf16 v[28:31], v[186:189], v[226:229], v[28:31]
	v_mfma_f32_16x16x32_bf16 v[16:19], v[152:155], v[234:237], v[16:19]
	v_mfma_f32_16x16x32_bf16 v[12:15], v[186:189], v[234:237], v[12:15]
	s_barrier
	s_setprio 0
	s_add_i32 s28, 0, 0x18000
	s_add_i32 s29, 0, 0x1c000
	v_add_u32_e32 v144, s28, v163
	v_add_u32_e32 v185, s29, v163
	ds_read_b128 v[132:135], v144
	ds_read_b128 v[136:139], v144 offset:1024
	ds_read_b128 v[140:143], v144 offset:2048
	ds_read_b128 v[144:147], v144 offset:3072
	ds_read_b128 v[148:151], v185
	ds_read_b128 v[152:155], v185 offset:1024
	ds_read_b128 v[178:181], v185 offset:2048
	ds_read_b128 v[186:189], v185 offset:3072
	s_add_u32 s26, s26, 0x100000
	s_addc_u32 s27, s27, 0
	s_mov_b32 m0, s51
	v_lshl_add_u64 v[244:245], s[26:27], 0, v[172:173]
	ds_read_b128 v[190:193], v184 offset:32768
	ds_read_b128 v[194:197], v184 offset:33792
	ds_read_b128 v[198:201], v184 offset:34816
	ds_read_b128 v[202:205], v184 offset:35840
	ds_read_b128 v[222:225], v184 offset:36864
	ds_read_b128 v[226:229], v184 offset:37888
	ds_read_b128 v[230:233], v184 offset:38912
	ds_read_b128 v[234:237], v184 offset:39936
	global_load_lds_dwordx4 v[244:245], off
	v_lshl_add_u64 v[244:245], s[26:27], 0, v[170:171]
	s_mov_b32 m0, s54
	s_nop 0
	global_load_lds_dwordx4 v[244:245], off
	s_waitcnt vmcnt(8)
	s_waitcnt lgkmcnt(0)
	s_setprio 1
	s_barrier
	v_mfma_f32_16x16x32_bf16 v[120:123], v[132:135], v[190:193], v[120:123]
	v_mfma_f32_16x16x32_bf16 v[116:119], v[140:143], v[190:193], v[116:119]
	v_mfma_f32_16x16x32_bf16 v[104:107], v[132:135], v[198:201], v[104:107]
	v_mfma_f32_16x16x32_bf16 v[100:103], v[140:143], v[198:201], v[100:103]
	v_mfma_f32_16x16x32_bf16 v[88:91], v[132:135], v[222:225], v[88:91]
	v_mfma_f32_16x16x32_bf16 v[84:87], v[140:143], v[222:225], v[84:87]
	v_mfma_f32_16x16x32_bf16 v[72:75], v[132:135], v[230:233], v[72:75]
	v_mfma_f32_16x16x32_bf16 v[68:71], v[140:143], v[230:233], v[68:71]
	v_mfma_f32_16x16x32_bf16 v[120:123], v[136:139], v[194:197], v[120:123]
	v_mfma_f32_16x16x32_bf16 v[116:119], v[144:147], v[194:197], v[116:119]
	v_mfma_f32_16x16x32_bf16 v[104:107], v[136:139], v[202:205], v[104:107]
	v_mfma_f32_16x16x32_bf16 v[100:103], v[144:147], v[202:205], v[100:103]
	v_mfma_f32_16x16x32_bf16 v[88:91], v[136:139], v[226:229], v[88:91]
	v_mfma_f32_16x16x32_bf16 v[84:87], v[144:147], v[226:229], v[84:87]
	v_mfma_f32_16x16x32_bf16 v[72:75], v[136:139], v[234:237], v[72:75]
	v_mfma_f32_16x16x32_bf16 v[68:71], v[144:147], v[234:237], v[68:71]
	v_mfma_f32_16x16x32_bf16 v[128:131], v[148:151], v[190:193], v[128:131]
	v_mfma_f32_16x16x32_bf16 v[124:127], v[178:181], v[190:193], v[124:127]
	v_mfma_f32_16x16x32_bf16 v[112:115], v[148:151], v[198:201], v[112:115]
	v_mfma_f32_16x16x32_bf16 v[108:111], v[178:181], v[198:201], v[108:111]
	v_mfma_f32_16x16x32_bf16 v[96:99], v[148:151], v[222:225], v[96:99]
	v_mfma_f32_16x16x32_bf16 v[92:95], v[178:181], v[222:225], v[92:95]
	v_mfma_f32_16x16x32_bf16 v[80:83], v[148:151], v[230:233], v[80:83]
	v_mfma_f32_16x16x32_bf16 v[76:79], v[178:181], v[230:233], v[76:79]
	v_mfma_f32_16x16x32_bf16 v[128:131], v[152:155], v[194:197], v[128:131]
	v_mfma_f32_16x16x32_bf16 v[124:127], v[186:189], v[194:197], v[124:127]
	v_mfma_f32_16x16x32_bf16 v[112:115], v[152:155], v[202:205], v[112:115]
	v_mfma_f32_16x16x32_bf16 v[108:111], v[186:189], v[202:205], v[108:111]
	v_mfma_f32_16x16x32_bf16 v[96:99], v[152:155], v[226:229], v[96:99]
	v_mfma_f32_16x16x32_bf16 v[92:95], v[186:189], v[226:229], v[92:95]
	v_mfma_f32_16x16x32_bf16 v[80:83], v[152:155], v[234:237], v[80:83]
	v_mfma_f32_16x16x32_bf16 v[76:79], v[186:189], v[234:237], v[76:79]
	s_barrier
	s_setprio 0
	s_add_i32 s26, s28, s1
	v_lshl_add_u64 v[182:183], v[182:183], 0, s[86:87]
	s_mov_b32 m0, s26
	ds_read_b128 v[190:193], v184 offset:49152
	ds_read_b128 v[194:197], v184 offset:50176
	ds_read_b128 v[198:201], v184 offset:51200
	ds_read_b128 v[202:205], v184 offset:52224
	ds_read_b128 v[222:225], v184 offset:53248
	ds_read_b128 v[226:229], v184 offset:54272
	ds_read_b128 v[230:233], v184 offset:55296
	ds_read_b128 v[234:237], v184 offset:56320
	global_load_lds_dwordx4 v[182:183], off
	s_add_i32 m0, s26, 0x2000
	s_add_u32 s24, s24, 0x100080
	v_lshl_add_u64 v[182:183], v[238:239], 0, s[86:87]
	s_addc_u32 s25, s25, 0
	s_add_i32 s26, s29, s1
	global_load_lds_dwordx4 v[182:183], off
	v_lshl_add_u64 v[182:183], s[24:25], 0, v[2:3]
	s_mov_b32 m0, s26
	s_nop 0
	global_load_lds_dwordx4 v[182:183], off
	v_lshl_add_u64 v[182:183], s[24:25], 0, v[168:169]
	s_add_i32 m0, s26, 0x2000
	s_nop 0
	global_load_lds_dwordx4 v[182:183], off
	v_lshl_add_u64 v[182:183], v[240:241], 0, s[86:87]
	s_mov_b32 m0, s78
	s_nop 0
	global_load_lds_dwordx4 v[182:183], off
	v_lshl_add_u64 v[182:183], v[242:243], 0, s[86:87]
	s_mov_b32 m0, s85
	s_nop 0
	global_load_lds_dwordx4 v[182:183], off
	s_waitcnt vmcnt(8)
	s_waitcnt lgkmcnt(0)
	s_setprio 1
	s_barrier
	v_mfma_f32_16x16x32_bf16 v[56:59], v[132:135], v[190:193], v[56:59]
	v_mfma_f32_16x16x32_bf16 v[52:55], v[140:143], v[190:193], v[52:55]
	v_mfma_f32_16x16x32_bf16 v[40:43], v[132:135], v[198:201], v[40:43]
	v_mfma_f32_16x16x32_bf16 v[36:39], v[140:143], v[198:201], v[36:39]
	v_mfma_f32_16x16x32_bf16 v[24:27], v[132:135], v[222:225], v[24:27]
	v_mfma_f32_16x16x32_bf16 v[20:23], v[140:143], v[222:225], v[20:23]
	v_mfma_f32_16x16x32_bf16 v[8:11], v[132:135], v[230:233], v[8:11]
	v_mfma_f32_16x16x32_bf16 v[4:7], v[140:143], v[230:233], v[4:7]
	v_mfma_f32_16x16x32_bf16 v[56:59], v[136:139], v[194:197], v[56:59]
	v_mfma_f32_16x16x32_bf16 v[52:55], v[144:147], v[194:197], v[52:55]
	v_mfma_f32_16x16x32_bf16 v[40:43], v[136:139], v[202:205], v[40:43]
	v_mfma_f32_16x16x32_bf16 v[36:39], v[144:147], v[202:205], v[36:39]
	v_mfma_f32_16x16x32_bf16 v[24:27], v[136:139], v[226:229], v[24:27]
	v_mfma_f32_16x16x32_bf16 v[20:23], v[144:147], v[226:229], v[20:23]
	v_mfma_f32_16x16x32_bf16 v[8:11], v[136:139], v[234:237], v[8:11]
	v_mfma_f32_16x16x32_bf16 v[4:7], v[144:147], v[234:237], v[4:7]
	v_mfma_f32_16x16x32_bf16 v[64:67], v[148:151], v[190:193], v[64:67]
	v_mfma_f32_16x16x32_bf16 v[60:63], v[178:181], v[190:193], v[60:63]
	v_mfma_f32_16x16x32_bf16 v[48:51], v[148:151], v[198:201], v[48:51]
	v_mfma_f32_16x16x32_bf16 v[44:47], v[178:181], v[198:201], v[44:47]
	v_mfma_f32_16x16x32_bf16 v[32:35], v[148:151], v[222:225], v[32:35]
	v_mfma_f32_16x16x32_bf16 v[28:31], v[178:181], v[222:225], v[28:31]
	v_mfma_f32_16x16x32_bf16 v[16:19], v[148:151], v[230:233], v[16:19]
	v_mfma_f32_16x16x32_bf16 v[12:15], v[178:181], v[230:233], v[12:15]
	v_mfma_f32_16x16x32_bf16 v[64:67], v[152:155], v[194:197], v[64:67]
	v_mfma_f32_16x16x32_bf16 v[60:63], v[186:189], v[194:197], v[60:63]
	v_mfma_f32_16x16x32_bf16 v[48:51], v[152:155], v[202:205], v[48:51]
	v_mfma_f32_16x16x32_bf16 v[44:47], v[186:189], v[202:205], v[44:47]
	v_mfma_f32_16x16x32_bf16 v[32:35], v[152:155], v[226:229], v[32:35]
	v_mfma_f32_16x16x32_bf16 v[28:31], v[186:189], v[226:229], v[28:31]
	v_mfma_f32_16x16x32_bf16 v[16:19], v[152:155], v[234:237], v[16:19]
	v_mfma_f32_16x16x32_bf16 v[12:15], v[186:189], v[234:237], v[12:15]
	s_barrier
	s_setprio 0
	s_add_i32 s58, s58, 2
	s_add_u32 s6, s6, 0x100
	s_addc_u32 s7, s7, 0
	s_add_u32 s21, s21, 0x100
	s_addc_u32 s13, s13, 0
	s_cmp_gt_u32 s58, 61
	s_cbranch_scc0 .LBB0_265
	s_and_b64 vcc, exec, s[30:31]
	s_cbranch_vccz .LBB0_268
	s_barrier

.LBB0_722:
	s_add_u32 s24, s51, s10
	s_addc_u32 s25, s52, s11
	s_add_u32 s24, s24, 0x2b800100
	s_addc_u32 s25, s25, 0
	s_add_u32 s28, s13, s10
	s_addc_u32 s29, s21, s11
	s_add_i32 s54, 0, 0x10000
	s_cmpk_eq_i32 s10, 0x1f00
	s_cselect_b32 s27, s9, s25
	s_cselect_b32 s26, s8, s24
	v_add_u32_e32 v145, s54, v143
	s_cselect_b32 s25, s7, s29
	s_cselect_b32 s24, s6, s28
	s_add_i32 s55, 0, 0x14000
	ds_read_b128 v[146:149], v145
	ds_read_b128 v[150:153], v145 offset:1024
	ds_read_b128 v[170:173], v145 offset:2048
	ds_read_b128 v[174:177], v145 offset:3072
	v_add_u32_e32 v145, s55, v143
	ds_read_b128 v[178:181], v145
	ds_read_b128 v[182:185], v145 offset:1024
	ds_read_b128 v[186:189], v145 offset:2048
	ds_read_b128 v[190:193], v145 offset:3072
	v_lshl_add_u64 v[154:155], v[138:139], 0, s[10:11]
	s_add_i32 m0, s5, 0xc000
	ds_read_b128 v[194:197], v144
	ds_read_b128 v[198:201], v144 offset:1024
	ds_read_b128 v[202:205], v144 offset:2048
	ds_read_b128 v[222:225], v144 offset:3072
	ds_read_b128 v[226:229], v144 offset:4096
	ds_read_b128 v[230:233], v144 offset:5120
	ds_read_b128 v[234:237], v144 offset:6144
	ds_read_b128 v[238:241], v144 offset:7168
	global_load_lds_dwordx4 v[154:155], off
	v_lshl_add_u64 v[154:155], v[140:141], 0, s[10:11]
	s_add_i32 m0, s5, 0xe000
	s_nop 0
	global_load_lds_dwordx4 v[154:155], off
	s_waitcnt vmcnt(8)
	s_waitcnt lgkmcnt(0)
	s_setprio 1
	s_barrier
	v_mfma_f32_16x16x32_bf16 v[128:131], v[146:149], v[194:197], v[128:131]
	v_mfma_f32_16x16x32_bf16 v[124:127], v[170:173], v[194:197], v[124:127]
	v_mfma_f32_16x16x32_bf16 v[116:119], v[146:149], v[202:205], v[116:119]
	v_mfma_f32_16x16x32_bf16 v[108:111], v[170:173], v[202:205], v[108:111]
	v_mfma_f32_16x16x32_bf16 v[100:103], v[146:149], v[226:229], v[100:103]
	v_mfma_f32_16x16x32_bf16 v[92:95], v[170:173], v[226:229], v[92:95]
	v_mfma_f32_16x16x32_bf16 v[84:87], v[146:149], v[234:237], v[84:87]
	v_mfma_f32_16x16x32_bf16 v[76:79], v[170:173], v[234:237], v[76:79]
	v_mfma_f32_16x16x32_bf16 v[128:131], v[150:153], v[198:201], v[128:131]
	v_mfma_f32_16x16x32_bf16 v[124:127], v[174:177], v[198:201], v[124:127]
	v_mfma_f32_16x16x32_bf16 v[116:119], v[150:153], v[222:225], v[116:119]
	v_mfma_f32_16x16x32_bf16 v[108:111], v[174:177], v[222:225], v[108:111]
	v_mfma_f32_16x16x32_bf16 v[100:103], v[150:153], v[230:233], v[100:103]
	v_mfma_f32_16x16x32_bf16 v[92:95], v[174:177], v[230:233], v[92:95]
	v_mfma_f32_16x16x32_bf16 v[84:87], v[150:153], v[238:241], v[84:87]
	v_mfma_f32_16x16x32_bf16 v[76:79], v[174:177], v[238:241], v[76:79]
	v_mfma_f32_16x16x32_bf16 v[120:123], v[178:181], v[194:197], v[120:123]
	v_mfma_f32_16x16x32_bf16 v[112:115], v[186:189], v[194:197], v[112:115]
	v_mfma_f32_16x16x32_bf16 v[104:107], v[178:181], v[202:205], v[104:107]
	v_mfma_f32_16x16x32_bf16 v[96:99], v[186:189], v[202:205], v[96:99]
	v_mfma_f32_16x16x32_bf16 v[88:91], v[178:181], v[226:229], v[88:91]
	v_mfma_f32_16x16x32_bf16 v[80:83], v[186:189], v[226:229], v[80:83]
	v_mfma_f32_16x16x32_bf16 v[72:75], v[178:181], v[234:237], v[72:75]
	v_mfma_f32_16x16x32_bf16 v[68:71], v[186:189], v[234:237], v[68:71]
	v_mfma_f32_16x16x32_bf16 v[120:123], v[182:185], v[198:201], v[120:123]
	v_mfma_f32_16x16x32_bf16 v[112:115], v[190:193], v[198:201], v[112:115]
	v_mfma_f32_16x16x32_bf16 v[104:107], v[182:185], v[222:225], v[104:107]
	v_mfma_f32_16x16x32_bf16 v[96:99], v[190:193], v[222:225], v[96:99]
	v_mfma_f32_16x16x32_bf16 v[88:91], v[182:185], v[230:233], v[88:91]
	v_mfma_f32_16x16x32_bf16 v[80:83], v[190:193], v[230:233], v[80:83]
	v_mfma_f32_16x16x32_bf16 v[72:75], v[182:185], v[238:241], v[72:75]
	v_mfma_f32_16x16x32_bf16 v[68:71], v[190:193], v[238:241], v[68:71]
	s_barrier
	s_setprio 0
	s_add_i32 s28, s54, s31
	v_lshl_add_u64 v[154:155], s[24:25], 0, v[2:3]
	s_mov_b32 m0, s28
	ds_read_b128 v[194:197], v144 offset:16384
	ds_read_b128 v[198:201], v144 offset:17408
	ds_read_b128 v[202:205], v144 offset:18432
	ds_read_b128 v[222:225], v144 offset:19456
	ds_read_b128 v[226:229], v144 offset:20480
	ds_read_b128 v[230:233], v144 offset:21504
	ds_read_b128 v[234:237], v144 offset:22528
	ds_read_b128 v[238:241], v144 offset:23552
	global_load_lds_dwordx4 v[154:155], off
	s_add_i32 m0, s28, 0x2000
	s_add_u32 s28, s24, 0x100000
	v_lshl_add_u64 v[242:243], s[24:25], 0, v[136:137]
	s_addc_u32 s29, s25, 0
	s_add_i32 s54, s55, s31
	global_load_lds_dwordx4 v[242:243], off
	v_lshl_add_u64 v[244:245], s[28:29], 0, v[2:3]
	s_mov_b32 m0, s54
	v_lshl_add_u64 v[246:247], s[26:27], 0, v[134:135]
	global_load_lds_dwordx4 v[244:245], off
	v_lshl_add_u64 v[244:245], s[28:29], 0, v[136:137]
	s_add_i32 m0, s54, 0x2000
	s_nop 0
	global_load_lds_dwordx4 v[244:245], off
	v_lshl_add_u64 v[244:245], s[26:27], 0, v[132:133]
	s_mov_b32 m0, s5
	s_nop 0
	global_load_lds_dwordx4 v[244:245], off
	s_mov_b32 m0, s35
	s_nop 0
	global_load_lds_dwordx4 v[246:247], off
	s_waitcnt vmcnt(8)
	s_waitcnt lgkmcnt(0)
	s_setprio 1
	s_barrier
	v_mfma_f32_16x16x32_bf16 v[64:67], v[146:149], v[194:197], v[64:67]
	v_mfma_f32_16x16x32_bf16 v[60:63], v[170:173], v[194:197], v[60:63]
	v_mfma_f32_16x16x32_bf16 v[52:55], v[146:149], v[202:205], v[52:55]
	v_mfma_f32_16x16x32_bf16 v[44:47], v[170:173], v[202:205], v[44:47]
	v_mfma_f32_16x16x32_bf16 v[36:39], v[146:149], v[226:229], v[36:39]
	v_mfma_f32_16x16x32_bf16 v[28:31], v[170:173], v[226:229], v[28:31]
	v_mfma_f32_16x16x32_bf16 v[20:23], v[146:149], v[234:237], v[20:23]
	v_mfma_f32_16x16x32_bf16 v[12:15], v[170:173], v[234:237], v[12:15]
	v_mfma_f32_16x16x32_bf16 v[64:67], v[150:153], v[198:201], v[64:67]
	v_mfma_f32_16x16x32_bf16 v[60:63], v[174:177], v[198:201], v[60:63]
	v_mfma_f32_16x16x32_bf16 v[52:55], v[150:153], v[222:225], v[52:55]
	v_mfma_f32_16x16x32_bf16 v[44:47], v[174:177], v[222:225], v[44:47]
	v_mfma_f32_16x16x32_bf16 v[36:39], v[150:153], v[230:233], v[36:39]
	v_mfma_f32_16x16x32_bf16 v[28:31], v[174:177], v[230:233], v[28:31]
	v_mfma_f32_16x16x32_bf16 v[20:23], v[150:153], v[238:241], v[20:23]
	v_mfma_f32_16x16x32_bf16 v[12:15], v[174:177], v[238:241], v[12:15]
	v_mfma_f32_16x16x32_bf16 v[56:59], v[178:181], v[194:197], v[56:59]
	v_mfma_f32_16x16x32_bf16 v[48:51], v[186:189], v[194:197], v[48:51]
	v_mfma_f32_16x16x32_bf16 v[40:43], v[178:181], v[202:205], v[40:43]
	v_mfma_f32_16x16x32_bf16 v[32:35], v[186:189], v[202:205], v[32:35]
	v_mfma_f32_16x16x32_bf16 v[24:27], v[178:181], v[226:229], v[24:27]
	v_mfma_f32_16x16x32_bf16 v[16:19], v[186:189], v[226:229], v[16:19]
	v_mfma_f32_16x16x32_bf16 v[8:11], v[178:181], v[234:237], v[8:11]
	v_mfma_f32_16x16x32_bf16 v[4:7], v[186:189], v[234:237], v[4:7]
	v_mfma_f32_16x16x32_bf16 v[56:59], v[182:185], v[198:201], v[56:59]
	v_mfma_f32_16x16x32_bf16 v[48:51], v[190:193], v[198:201], v[48:51]
	v_mfma_f32_16x16x32_bf16 v[40:43], v[182:185], v[222:225], v[40:43]
	v_mfma_f32_16x16x32_bf16 v[32:35], v[190:193], v[222:225], v[32:35]
	v_mfma_f32_16x16x32_bf16 v[24:27], v[182:185], v[230:233], v[24:27]
	v_mfma_f32_16x16x32_bf16 v[16:19], v[190:193], v[230:233], v[16:19]
	v_mfma_f32_16x16x32_bf16 v[8:11], v[182:185], v[238:241], v[8:11]
	v_mfma_f32_16x16x32_bf16 v[4:7], v[190:193], v[238:241], v[4:7]
	s_barrier
	s_setprio 0
	s_add_i32 s28, 0, 0x18000
	v_add_u32_e32 v145, s28, v143
	s_add_i32 s29, 0, 0x1c000
	ds_read_b128 v[146:149], v145
	ds_read_b128 v[150:153], v145 offset:1024
	ds_read_b128 v[170:173], v145 offset:2048
	ds_read_b128 v[174:177], v145 offset:3072
	v_add_u32_e32 v145, s29, v143
	ds_read_b128 v[178:181], v145
	ds_read_b128 v[182:185], v145 offset:1024
	ds_read_b128 v[186:189], v145 offset:2048
	ds_read_b128 v[190:193], v145 offset:3072
	s_add_u32 s26, s26, 0x100000
	s_addc_u32 s27, s27, 0
	s_mov_b32 m0, s38
	v_lshl_add_u64 v[248:249], s[26:27], 0, v[132:133]
	ds_read_b128 v[194:197], v144 offset:32768
	ds_read_b128 v[198:201], v144 offset:33792
	ds_read_b128 v[202:205], v144 offset:34816
	ds_read_b128 v[222:225], v144 offset:35840
	ds_read_b128 v[226:229], v144 offset:36864
	ds_read_b128 v[230:233], v144 offset:37888
	ds_read_b128 v[234:237], v144 offset:38912
	ds_read_b128 v[238:241], v144 offset:39936
	global_load_lds_dwordx4 v[248:249], off
	v_lshl_add_u64 v[248:249], s[26:27], 0, v[134:135]
	s_mov_b32 m0, s42
	s_nop 0
	global_load_lds_dwordx4 v[248:249], off
	s_waitcnt vmcnt(8)
	s_waitcnt lgkmcnt(0)
	s_setprio 1
	s_barrier
	v_mfma_f32_16x16x32_bf16 v[128:131], v[146:149], v[194:197], v[128:131]
	v_mfma_f32_16x16x32_bf16 v[124:127], v[170:173], v[194:197], v[124:127]
	v_mfma_f32_16x16x32_bf16 v[116:119], v[146:149], v[202:205], v[116:119]
	v_mfma_f32_16x16x32_bf16 v[108:111], v[170:173], v[202:205], v[108:111]
	v_mfma_f32_16x16x32_bf16 v[100:103], v[146:149], v[226:229], v[100:103]
	v_mfma_f32_16x16x32_bf16 v[92:95], v[170:173], v[226:229], v[92:95]
	v_mfma_f32_16x16x32_bf16 v[84:87], v[146:149], v[234:237], v[84:87]
	v_mfma_f32_16x16x32_bf16 v[76:79], v[170:173], v[234:237], v[76:79]
	v_mfma_f32_16x16x32_bf16 v[128:131], v[150:153], v[198:201], v[128:131]
	v_mfma_f32_16x16x32_bf16 v[124:127], v[174:177], v[198:201], v[124:127]
	v_mfma_f32_16x16x32_bf16 v[116:119], v[150:153], v[222:225], v[116:119]
	v_mfma_f32_16x16x32_bf16 v[108:111], v[174:177], v[222:225], v[108:111]
	v_mfma_f32_16x16x32_bf16 v[100:103], v[150:153], v[230:233], v[100:103]
	v_mfma_f32_16x16x32_bf16 v[92:95], v[174:177], v[230:233], v[92:95]
	v_mfma_f32_16x16x32_bf16 v[84:87], v[150:153], v[238:241], v[84:87]
	v_mfma_f32_16x16x32_bf16 v[76:79], v[174:177], v[238:241], v[76:79]
	v_mfma_f32_16x16x32_bf16 v[120:123], v[178:181], v[194:197], v[120:123]
	v_mfma_f32_16x16x32_bf16 v[112:115], v[186:189], v[194:197], v[112:115]
	v_mfma_f32_16x16x32_bf16 v[104:107], v[178:181], v[202:205], v[104:107]
	v_mfma_f32_16x16x32_bf16 v[96:99], v[186:189], v[202:205], v[96:99]
	v_mfma_f32_16x16x32_bf16 v[88:91], v[178:181], v[226:229], v[88:91]
	v_mfma_f32_16x16x32_bf16 v[80:83], v[186:189], v[226:229], v[80:83]
	v_mfma_f32_16x16x32_bf16 v[72:75], v[178:181], v[234:237], v[72:75]
	v_mfma_f32_16x16x32_bf16 v[68:71], v[186:189], v[234:237], v[68:71]
	v_mfma_f32_16x16x32_bf16 v[120:123], v[182:185], v[198:201], v[120:123]
	v_mfma_f32_16x16x32_bf16 v[112:115], v[190:193], v[198:201], v[112:115]
	v_mfma_f32_16x16x32_bf16 v[104:107], v[182:185], v[222:225], v[104:107]
	v_mfma_f32_16x16x32_bf16 v[96:99], v[190:193], v[222:225], v[96:99]
	v_mfma_f32_16x16x32_bf16 v[88:91], v[182:185], v[230:233], v[88:91]
	v_mfma_f32_16x16x32_bf16 v[80:83], v[190:193], v[230:233], v[80:83]
	v_mfma_f32_16x16x32_bf16 v[72:75], v[182:185], v[238:241], v[72:75]
	v_mfma_f32_16x16x32_bf16 v[68:71], v[190:193], v[238:241], v[68:71]
	s_barrier
	s_setprio 0
	s_add_i32 s26, s28, s31
	v_lshl_add_u64 v[154:155], v[154:155], 0, s[86:87]
	s_mov_b32 m0, s26
	ds_read_b128 v[194:197], v144 offset:49152
	ds_read_b128 v[198:201], v144 offset:50176
	ds_read_b128 v[202:205], v144 offset:51200
	ds_read_b128 v[222:225], v144 offset:52224
	ds_read_b128 v[226:229], v144 offset:53248
	ds_read_b128 v[230:233], v144 offset:54272
	ds_read_b128 v[234:237], v144 offset:55296
	ds_read_b128 v[238:241], v144 offset:56320
	global_load_lds_dwordx4 v[154:155], off
	s_add_i32 m0, s26, 0x2000
	s_add_u32 s24, s24, 0x100080
	v_lshl_add_u64 v[154:155], v[242:243], 0, s[86:87]
	s_addc_u32 s25, s25, 0
	s_add_i32 s26, s29, s31
	global_load_lds_dwordx4 v[154:155], off
	v_lshl_add_u64 v[154:155], s[24:25], 0, v[2:3]
	s_mov_b32 m0, s26
	s_nop 0
	global_load_lds_dwordx4 v[154:155], off
	v_lshl_add_u64 v[154:155], s[24:25], 0, v[136:137]
	s_add_i32 m0, s26, 0x2000
	s_nop 0
	global_load_lds_dwordx4 v[154:155], off
	v_lshl_add_u64 v[154:155], v[244:245], 0, s[86:87]
	s_mov_b32 m0, s46
	s_nop 0
	global_load_lds_dwordx4 v[154:155], off
	v_lshl_add_u64 v[154:155], v[246:247], 0, s[86:87]
	s_mov_b32 m0, s50
	s_nop 0
	global_load_lds_dwordx4 v[154:155], off
	s_waitcnt vmcnt(8)
	s_waitcnt lgkmcnt(0)
	s_setprio 1
	s_barrier
	v_mfma_f32_16x16x32_bf16 v[64:67], v[146:149], v[194:197], v[64:67]
	v_mfma_f32_16x16x32_bf16 v[60:63], v[170:173], v[194:197], v[60:63]
	v_mfma_f32_16x16x32_bf16 v[52:55], v[146:149], v[202:205], v[52:55]
	v_mfma_f32_16x16x32_bf16 v[44:47], v[170:173], v[202:205], v[44:47]
	v_mfma_f32_16x16x32_bf16 v[36:39], v[146:149], v[226:229], v[36:39]
	v_mfma_f32_16x16x32_bf16 v[28:31], v[170:173], v[226:229], v[28:31]
	v_mfma_f32_16x16x32_bf16 v[20:23], v[146:149], v[234:237], v[20:23]
	v_mfma_f32_16x16x32_bf16 v[12:15], v[170:173], v[234:237], v[12:15]
	v_mfma_f32_16x16x32_bf16 v[64:67], v[150:153], v[198:201], v[64:67]
	v_mfma_f32_16x16x32_bf16 v[60:63], v[174:177], v[198:201], v[60:63]
	v_mfma_f32_16x16x32_bf16 v[52:55], v[150:153], v[222:225], v[52:55]
	v_mfma_f32_16x16x32_bf16 v[44:47], v[174:177], v[222:225], v[44:47]
	v_mfma_f32_16x16x32_bf16 v[36:39], v[150:153], v[230:233], v[36:39]
	v_mfma_f32_16x16x32_bf16 v[28:31], v[174:177], v[230:233], v[28:31]
	v_mfma_f32_16x16x32_bf16 v[20:23], v[150:153], v[238:241], v[20:23]
	v_mfma_f32_16x16x32_bf16 v[12:15], v[174:177], v[238:241], v[12:15]
	v_mfma_f32_16x16x32_bf16 v[56:59], v[178:181], v[194:197], v[56:59]
	v_mfma_f32_16x16x32_bf16 v[48:51], v[186:189], v[194:197], v[48:51]
	v_mfma_f32_16x16x32_bf16 v[40:43], v[178:181], v[202:205], v[40:43]
	v_mfma_f32_16x16x32_bf16 v[32:35], v[186:189], v[202:205], v[32:35]
	v_mfma_f32_16x16x32_bf16 v[24:27], v[178:181], v[226:229], v[24:27]
	v_mfma_f32_16x16x32_bf16 v[16:19], v[186:189], v[226:229], v[16:19]
	v_mfma_f32_16x16x32_bf16 v[8:11], v[178:181], v[234:237], v[8:11]
	v_mfma_f32_16x16x32_bf16 v[4:7], v[186:189], v[234:237], v[4:7]
	v_mfma_f32_16x16x32_bf16 v[56:59], v[182:185], v[198:201], v[56:59]
	v_mfma_f32_16x16x32_bf16 v[48:51], v[190:193], v[198:201], v[48:51]
	v_mfma_f32_16x16x32_bf16 v[40:43], v[182:185], v[222:225], v[40:43]
	v_mfma_f32_16x16x32_bf16 v[32:35], v[190:193], v[222:225], v[32:35]
	v_mfma_f32_16x16x32_bf16 v[24:27], v[182:185], v[230:233], v[24:27]
	v_mfma_f32_16x16x32_bf16 v[16:19], v[190:193], v[230:233], v[16:19]
	v_mfma_f32_16x16x32_bf16 v[8:11], v[182:185], v[238:241], v[8:11]
	v_mfma_f32_16x16x32_bf16 v[4:7], v[190:193], v[238:241], v[4:7]
	s_barrier
	s_setprio 0
	s_add_i32 s53, s53, 2
	s_add_u32 s10, s10, 0x100
	s_addc_u32 s11, s11, 0
	s_cmp_gt_u32 s53, 61
	s_cbranch_scc0 .LBB0_722
	s_cmpk_lt_u32 s23, 0x100
	s_cbranch_scc0 .LBB0_725
	s_barrier

.LBB0_1202:
	s_add_u32 s24, s6, 0xfff00080
	s_addc_u32 s25, s7, -1
	s_add_i32 s28, 0, 0x10000
	s_cmp_eq_u32 s58, 60
	s_cselect_b32 s27, s35, s25
	s_cselect_b32 s26, s53, s24
	s_cselect_b32 s25, s31, s13
	s_cselect_b32 s24, s92, s21
	s_add_i32 s71, 0, 0x14000
	v_add_u32_e32 v150, s28, v163
	v_add_u32_e32 v154, s71, v163
	ds_read_b128 v[138:141], v150
	ds_read_b128 v[142:145], v150 offset:1024
	ds_read_b128 v[146:149], v150 offset:2048
	ds_read_b128 v[150:153], v150 offset:3072
	ds_read_b128 v[168:171], v154
	ds_read_b128 v[172:175], v154 offset:1024
	ds_read_b128 v[176:179], v154 offset:2048
	ds_read_b128 v[180:183], v154 offset:3072
	v_lshl_add_u64 v[154:155], s[6:7], 0, v[134:135]
	s_add_i32 m0, s50, 0xc000
	ds_read_b128 v[188:191], v186
	ds_read_b128 v[192:195], v186 offset:1024
	ds_read_b128 v[196:199], v186 offset:2048
	ds_read_b128 v[200:203], v186 offset:3072
	ds_read_b128 v[222:225], v186 offset:4096
	ds_read_b128 v[226:229], v186 offset:5120
	ds_read_b128 v[230:233], v186 offset:6144
	ds_read_b128 v[234:237], v186 offset:7168
	global_load_lds_dwordx4 v[154:155], off
	v_lshl_add_u64 v[154:155], s[6:7], 0, v[136:137]
	s_add_i32 m0, s50, 0xe000
	s_nop 0
	global_load_lds_dwordx4 v[154:155], off
	s_waitcnt vmcnt(8)
	s_waitcnt lgkmcnt(0)
	s_setprio 1
	s_barrier
	v_mfma_f32_16x16x32_bf16 v[128:131], v[138:141], v[188:191], v[128:131]
	v_mfma_f32_16x16x32_bf16 v[124:127], v[146:149], v[188:191], v[124:127]
	v_mfma_f32_16x16x32_bf16 v[112:115], v[138:141], v[196:199], v[112:115]
	v_mfma_f32_16x16x32_bf16 v[108:111], v[146:149], v[196:199], v[108:111]
	v_mfma_f32_16x16x32_bf16 v[96:99], v[138:141], v[222:225], v[96:99]
	v_mfma_f32_16x16x32_bf16 v[92:95], v[146:149], v[222:225], v[92:95]
	v_mfma_f32_16x16x32_bf16 v[80:83], v[138:141], v[230:233], v[80:83]
	v_mfma_f32_16x16x32_bf16 v[76:79], v[146:149], v[230:233], v[76:79]
	v_mfma_f32_16x16x32_bf16 v[128:131], v[142:145], v[192:195], v[128:131]
	v_mfma_f32_16x16x32_bf16 v[124:127], v[150:153], v[192:195], v[124:127]
	v_mfma_f32_16x16x32_bf16 v[112:115], v[142:145], v[200:203], v[112:115]
	v_mfma_f32_16x16x32_bf16 v[108:111], v[150:153], v[200:203], v[108:111]
	v_mfma_f32_16x16x32_bf16 v[96:99], v[142:145], v[226:229], v[96:99]
	v_mfma_f32_16x16x32_bf16 v[92:95], v[150:153], v[226:229], v[92:95]
	v_mfma_f32_16x16x32_bf16 v[80:83], v[142:145], v[234:237], v[80:83]
	v_mfma_f32_16x16x32_bf16 v[76:79], v[150:153], v[234:237], v[76:79]
	v_mfma_f32_16x16x32_bf16 v[120:123], v[168:171], v[188:191], v[120:123]
	v_mfma_f32_16x16x32_bf16 v[116:119], v[176:179], v[188:191], v[116:119]
	v_mfma_f32_16x16x32_bf16 v[104:107], v[168:171], v[196:199], v[104:107]
	v_mfma_f32_16x16x32_bf16 v[100:103], v[176:179], v[196:199], v[100:103]
	v_mfma_f32_16x16x32_bf16 v[88:91], v[168:171], v[222:225], v[88:91]
	v_mfma_f32_16x16x32_bf16 v[84:87], v[176:179], v[222:225], v[84:87]
	v_mfma_f32_16x16x32_bf16 v[72:75], v[168:171], v[230:233], v[72:75]
	v_mfma_f32_16x16x32_bf16 v[68:71], v[176:179], v[230:233], v[68:71]
	v_mfma_f32_16x16x32_bf16 v[120:123], v[172:175], v[192:195], v[120:123]
	v_mfma_f32_16x16x32_bf16 v[116:119], v[180:183], v[192:195], v[116:119]
	v_mfma_f32_16x16x32_bf16 v[104:107], v[172:175], v[200:203], v[104:107]
	v_mfma_f32_16x16x32_bf16 v[100:103], v[180:183], v[200:203], v[100:103]
	v_mfma_f32_16x16x32_bf16 v[88:91], v[172:175], v[226:229], v[88:91]
	v_mfma_f32_16x16x32_bf16 v[84:87], v[180:183], v[226:229], v[84:87]
	v_mfma_f32_16x16x32_bf16 v[72:75], v[172:175], v[234:237], v[72:75]
	v_mfma_f32_16x16x32_bf16 v[68:71], v[180:183], v[234:237], v[68:71]
	s_barrier
	s_setprio 0
	s_add_i32 s28, s28, s46
	v_lshl_add_u64 v[154:155], s[24:25], 0, v[2:3]
	s_mov_b32 m0, s28
	ds_read_b128 v[188:191], v186 offset:16384
	ds_read_b128 v[192:195], v186 offset:17408
	ds_read_b128 v[196:199], v186 offset:18432
	ds_read_b128 v[200:203], v186 offset:19456
	ds_read_b128 v[222:225], v186 offset:20480
	ds_read_b128 v[226:229], v186 offset:21504
	ds_read_b128 v[230:233], v186 offset:22528
	ds_read_b128 v[234:237], v186 offset:23552
	global_load_lds_dwordx4 v[154:155], off
	s_add_i32 m0, s28, 0x2000
	s_add_u32 s28, s24, 0x100000
	v_lshl_add_u64 v[184:185], s[24:25], 0, v[132:133]
	s_addc_u32 s29, s25, 0
	s_add_i32 s71, s71, s46
	global_load_lds_dwordx4 v[184:185], off
	v_lshl_add_u64 v[204:205], s[28:29], 0, v[2:3]
	s_mov_b32 m0, s71
	v_lshl_add_u64 v[238:239], s[26:27], 0, v[132:133]
	global_load_lds_dwordx4 v[204:205], off
	v_lshl_add_u64 v[204:205], s[28:29], 0, v[132:133]
	s_add_i32 m0, s71, 0x2000
	s_nop 0
	global_load_lds_dwordx4 v[204:205], off
	v_lshl_add_u64 v[204:205], s[26:27], 0, v[2:3]
	s_mov_b32 m0, s50
	s_nop 0
	global_load_lds_dwordx4 v[204:205], off
	s_mov_b32 m0, s23
	s_nop 0
	global_load_lds_dwordx4 v[238:239], off
	s_waitcnt vmcnt(8)
	s_waitcnt lgkmcnt(0)
	s_setprio 1
	s_barrier
	v_mfma_f32_16x16x32_bf16 v[64:67], v[138:141], v[188:191], v[64:67]
	v_mfma_f32_16x16x32_bf16 v[60:63], v[146:149], v[188:191], v[60:63]
	v_mfma_f32_16x16x32_bf16 v[48:51], v[138:141], v[196:199], v[48:51]
	v_mfma_f32_16x16x32_bf16 v[44:47], v[146:149], v[196:199], v[44:47]
	v_mfma_f32_16x16x32_bf16 v[32:35], v[138:141], v[222:225], v[32:35]
	v_mfma_f32_16x16x32_bf16 v[28:31], v[146:149], v[222:225], v[28:31]
	v_mfma_f32_16x16x32_bf16 v[16:19], v[138:141], v[230:233], v[16:19]
	v_mfma_f32_16x16x32_bf16 v[12:15], v[146:149], v[230:233], v[12:15]
	v_mfma_f32_16x16x32_bf16 v[64:67], v[142:145], v[192:195], v[64:67]
	v_mfma_f32_16x16x32_bf16 v[60:63], v[150:153], v[192:195], v[60:63]
	v_mfma_f32_16x16x32_bf16 v[48:51], v[142:145], v[200:203], v[48:51]
	v_mfma_f32_16x16x32_bf16 v[44:47], v[150:153], v[200:203], v[44:47]
	v_mfma_f32_16x16x32_bf16 v[32:35], v[142:145], v[226:229], v[32:35]
	v_mfma_f32_16x16x32_bf16 v[28:31], v[150:153], v[226:229], v[28:31]
	v_mfma_f32_16x16x32_bf16 v[16:19], v[142:145], v[234:237], v[16:19]
	v_mfma_f32_16x16x32_bf16 v[12:15], v[150:153], v[234:237], v[12:15]
	v_mfma_f32_16x16x32_bf16 v[56:59], v[168:171], v[188:191], v[56:59]
	v_mfma_f32_16x16x32_bf16 v[52:55], v[176:179], v[188:191], v[52:55]
	v_mfma_f32_16x16x32_bf16 v[40:43], v[168:171], v[196:199], v[40:43]
	v_mfma_f32_16x16x32_bf16 v[36:39], v[176:179], v[196:199], v[36:39]
	v_mfma_f32_16x16x32_bf16 v[24:27], v[168:171], v[222:225], v[24:27]
	v_mfma_f32_16x16x32_bf16 v[20:23], v[176:179], v[222:225], v[20:23]
	v_mfma_f32_16x16x32_bf16 v[8:11], v[168:171], v[230:233], v[8:11]
	v_mfma_f32_16x16x32_bf16 v[4:7], v[176:179], v[230:233], v[4:7]
	v_mfma_f32_16x16x32_bf16 v[56:59], v[172:175], v[192:195], v[56:59]
	v_mfma_f32_16x16x32_bf16 v[52:55], v[180:183], v[192:195], v[52:55]
	v_mfma_f32_16x16x32_bf16 v[40:43], v[172:175], v[200:203], v[40:43]
	v_mfma_f32_16x16x32_bf16 v[36:39], v[180:183], v[200:203], v[36:39]
	v_mfma_f32_16x16x32_bf16 v[24:27], v[172:175], v[226:229], v[24:27]
	v_mfma_f32_16x16x32_bf16 v[20:23], v[180:183], v[226:229], v[20:23]
	v_mfma_f32_16x16x32_bf16 v[8:11], v[172:175], v[234:237], v[8:11]
	v_mfma_f32_16x16x32_bf16 v[4:7], v[180:183], v[234:237], v[4:7]
	s_barrier
	s_setprio 0
	s_add_i32 s28, 0, 0x18000
	s_add_i32 s29, 0, 0x1c000
	v_add_u32_e32 v150, s28, v163
	v_add_u32_e32 v180, s29, v163
	ds_read_b128 v[138:141], v150
	ds_read_b128 v[142:145], v150 offset:1024
	ds_read_b128 v[146:149], v150 offset:2048
	ds_read_b128 v[150:153], v150 offset:3072
	ds_read_b128 v[168:171], v180
	ds_read_b128 v[172:175], v180 offset:1024
	ds_read_b128 v[176:179], v180 offset:2048
	ds_read_b128 v[180:183], v180 offset:3072
	s_add_u32 s26, s26, 0x100000
	s_addc_u32 s27, s27, 0
	s_mov_b32 m0, s51
	v_lshl_add_u64 v[240:241], s[26:27], 0, v[2:3]
	ds_read_b128 v[188:191], v186 offset:32768
	ds_read_b128 v[192:195], v186 offset:33792
	ds_read_b128 v[196:199], v186 offset:34816
	ds_read_b128 v[200:203], v186 offset:35840
	ds_read_b128 v[222:225], v186 offset:36864
	ds_read_b128 v[226:229], v186 offset:37888
	ds_read_b128 v[230:233], v186 offset:38912
	ds_read_b128 v[234:237], v186 offset:39936
	global_load_lds_dwordx4 v[240:241], off
	v_lshl_add_u64 v[240:241], s[26:27], 0, v[132:133]
	s_mov_b32 m0, s54
	s_nop 0
	global_load_lds_dwordx4 v[240:241], off
	s_waitcnt vmcnt(8)
	s_waitcnt lgkmcnt(0)
	s_setprio 1
	s_barrier
	v_mfma_f32_16x16x32_bf16 v[128:131], v[138:141], v[188:191], v[128:131]
	v_mfma_f32_16x16x32_bf16 v[124:127], v[146:149], v[188:191], v[124:127]
	v_mfma_f32_16x16x32_bf16 v[112:115], v[138:141], v[196:199], v[112:115]
	v_mfma_f32_16x16x32_bf16 v[108:111], v[146:149], v[196:199], v[108:111]
	v_mfma_f32_16x16x32_bf16 v[96:99], v[138:141], v[222:225], v[96:99]
	v_mfma_f32_16x16x32_bf16 v[92:95], v[146:149], v[222:225], v[92:95]
	v_mfma_f32_16x16x32_bf16 v[80:83], v[138:141], v[230:233], v[80:83]
	v_mfma_f32_16x16x32_bf16 v[76:79], v[146:149], v[230:233], v[76:79]
	v_mfma_f32_16x16x32_bf16 v[128:131], v[142:145], v[192:195], v[128:131]
	v_mfma_f32_16x16x32_bf16 v[124:127], v[150:153], v[192:195], v[124:127]
	v_mfma_f32_16x16x32_bf16 v[112:115], v[142:145], v[200:203], v[112:115]
	v_mfma_f32_16x16x32_bf16 v[108:111], v[150:153], v[200:203], v[108:111]
	v_mfma_f32_16x16x32_bf16 v[96:99], v[142:145], v[226:229], v[96:99]
	v_mfma_f32_16x16x32_bf16 v[92:95], v[150:153], v[226:229], v[92:95]
	v_mfma_f32_16x16x32_bf16 v[80:83], v[142:145], v[234:237], v[80:83]
	v_mfma_f32_16x16x32_bf16 v[76:79], v[150:153], v[234:237], v[76:79]
	v_mfma_f32_16x16x32_bf16 v[120:123], v[168:171], v[188:191], v[120:123]
	v_mfma_f32_16x16x32_bf16 v[116:119], v[176:179], v[188:191], v[116:119]
	v_mfma_f32_16x16x32_bf16 v[104:107], v[168:171], v[196:199], v[104:107]
	v_mfma_f32_16x16x32_bf16 v[100:103], v[176:179], v[196:199], v[100:103]
	v_mfma_f32_16x16x32_bf16 v[88:91], v[168:171], v[222:225], v[88:91]
	v_mfma_f32_16x16x32_bf16 v[84:87], v[176:179], v[222:225], v[84:87]
	v_mfma_f32_16x16x32_bf16 v[72:75], v[168:171], v[230:233], v[72:75]
	v_mfma_f32_16x16x32_bf16 v[68:71], v[176:179], v[230:233], v[68:71]
	v_mfma_f32_16x16x32_bf16 v[120:123], v[172:175], v[192:195], v[120:123]
	v_mfma_f32_16x16x32_bf16 v[116:119], v[180:183], v[192:195], v[116:119]
	v_mfma_f32_16x16x32_bf16 v[104:107], v[172:175], v[200:203], v[104:107]
	v_mfma_f32_16x16x32_bf16 v[100:103], v[180:183], v[200:203], v[100:103]
	v_mfma_f32_16x16x32_bf16 v[88:91], v[172:175], v[226:229], v[88:91]
	v_mfma_f32_16x16x32_bf16 v[84:87], v[180:183], v[226:229], v[84:87]
	v_mfma_f32_16x16x32_bf16 v[72:75], v[172:175], v[234:237], v[72:75]
	v_mfma_f32_16x16x32_bf16 v[68:71], v[180:183], v[234:237], v[68:71]
	s_barrier
	s_setprio 0
	s_add_i32 s26, s28, s46
	v_lshl_add_u64 v[154:155], v[154:155], 0, s[86:87]
	s_mov_b32 m0, s26
	ds_read_b128 v[188:191], v186 offset:49152
	ds_read_b128 v[192:195], v186 offset:50176
	ds_read_b128 v[196:199], v186 offset:51200
	ds_read_b128 v[200:203], v186 offset:52224
	ds_read_b128 v[222:225], v186 offset:53248
	ds_read_b128 v[226:229], v186 offset:54272
	ds_read_b128 v[230:233], v186 offset:55296
	ds_read_b128 v[234:237], v186 offset:56320
	global_load_lds_dwordx4 v[154:155], off
	s_add_i32 m0, s26, 0x2000
	s_add_u32 s24, s24, 0x100080
	v_lshl_add_u64 v[154:155], v[184:185], 0, s[86:87]
	s_addc_u32 s25, s25, 0
	s_add_i32 s26, s29, s46
	global_load_lds_dwordx4 v[154:155], off
	v_lshl_add_u64 v[154:155], s[24:25], 0, v[2:3]
	s_mov_b32 m0, s26
	s_nop 0
	global_load_lds_dwordx4 v[154:155], off
	v_lshl_add_u64 v[154:155], s[24:25], 0, v[132:133]
	s_add_i32 m0, s26, 0x2000
	s_nop 0
	global_load_lds_dwordx4 v[154:155], off
	v_lshl_add_u64 v[154:155], v[204:205], 0, s[86:87]
	s_mov_b32 m0, s76
	s_nop 0
	global_load_lds_dwordx4 v[154:155], off
	v_lshl_add_u64 v[154:155], v[238:239], 0, s[86:87]
	s_mov_b32 m0, s77
	s_nop 0
	global_load_lds_dwordx4 v[154:155], off
	s_waitcnt vmcnt(8)
	s_waitcnt lgkmcnt(0)
	s_setprio 1
	s_barrier
	v_mfma_f32_16x16x32_bf16 v[64:67], v[138:141], v[188:191], v[64:67]
	v_mfma_f32_16x16x32_bf16 v[60:63], v[146:149], v[188:191], v[60:63]
	v_mfma_f32_16x16x32_bf16 v[48:51], v[138:141], v[196:199], v[48:51]
	v_mfma_f32_16x16x32_bf16 v[44:47], v[146:149], v[196:199], v[44:47]
	v_mfma_f32_16x16x32_bf16 v[32:35], v[138:141], v[222:225], v[32:35]
	v_mfma_f32_16x16x32_bf16 v[28:31], v[146:149], v[222:225], v[28:31]
	v_mfma_f32_16x16x32_bf16 v[16:19], v[138:141], v[230:233], v[16:19]
	v_mfma_f32_16x16x32_bf16 v[12:15], v[146:149], v[230:233], v[12:15]
	v_mfma_f32_16x16x32_bf16 v[64:67], v[142:145], v[192:195], v[64:67]
	v_mfma_f32_16x16x32_bf16 v[60:63], v[150:153], v[192:195], v[60:63]
	v_mfma_f32_16x16x32_bf16 v[48:51], v[142:145], v[200:203], v[48:51]
	v_mfma_f32_16x16x32_bf16 v[44:47], v[150:153], v[200:203], v[44:47]
	v_mfma_f32_16x16x32_bf16 v[32:35], v[142:145], v[226:229], v[32:35]
	v_mfma_f32_16x16x32_bf16 v[28:31], v[150:153], v[226:229], v[28:31]
	v_mfma_f32_16x16x32_bf16 v[16:19], v[142:145], v[234:237], v[16:19]
	v_mfma_f32_16x16x32_bf16 v[12:15], v[150:153], v[234:237], v[12:15]
	v_mfma_f32_16x16x32_bf16 v[56:59], v[168:171], v[188:191], v[56:59]
	v_mfma_f32_16x16x32_bf16 v[52:55], v[176:179], v[188:191], v[52:55]
	v_mfma_f32_16x16x32_bf16 v[40:43], v[168:171], v[196:199], v[40:43]
	v_mfma_f32_16x16x32_bf16 v[36:39], v[176:179], v[196:199], v[36:39]
	v_mfma_f32_16x16x32_bf16 v[24:27], v[168:171], v[222:225], v[24:27]
	v_mfma_f32_16x16x32_bf16 v[20:23], v[176:179], v[222:225], v[20:23]
	v_mfma_f32_16x16x32_bf16 v[8:11], v[168:171], v[230:233], v[8:11]
	v_mfma_f32_16x16x32_bf16 v[4:7], v[176:179], v[230:233], v[4:7]
	v_mfma_f32_16x16x32_bf16 v[56:59], v[172:175], v[192:195], v[56:59]
	v_mfma_f32_16x16x32_bf16 v[52:55], v[180:183], v[192:195], v[52:55]
	v_mfma_f32_16x16x32_bf16 v[40:43], v[172:175], v[200:203], v[40:43]
	v_mfma_f32_16x16x32_bf16 v[36:39], v[180:183], v[200:203], v[36:39]
	v_mfma_f32_16x16x32_bf16 v[24:27], v[172:175], v[226:229], v[24:27]
	v_mfma_f32_16x16x32_bf16 v[20:23], v[180:183], v[226:229], v[20:23]
	v_mfma_f32_16x16x32_bf16 v[8:11], v[172:175], v[234:237], v[8:11]
	v_mfma_f32_16x16x32_bf16 v[4:7], v[180:183], v[234:237], v[4:7]
	s_barrier
	s_setprio 0
	s_add_i32 s58, s58, 2
	s_add_u32 s6, s6, 0x100
	s_addc_u32 s7, s7, 0
	s_add_u32 s21, s21, 0x100
	s_addc_u32 s13, s13, 0
	s_cmp_gt_u32 s58, 61
	s_cbranch_scc0 .LBB0_1202
	s_and_b64 vcc, exec, s[14:15]
	s_cbranch_vccz .LBB0_1205
	s_barrier
